# read wide: mixer C bias fragments by ds_read_b64 from a parity-split second table copy in static LDS (on top of the mixer A change)
# speedup vs baseline: 1.0027x; 1.0027x over previous
; __device__ __forceinline__ void mixer_c_shared(const bf16* CQ, const bf16* CK, const bf16* CV  , bf16* O, const float* rel_bias, const float* sink, LAS unsigned char* lds, int G, int blk, int tid, int lane, int wave) {
;     ...
;         for (int idx = tid; idx < TC_LEN; idx += NWAVES * 64) { const int i = idx - TC_OFF; const bool in = (i >= 0 && i <= 256); const int bk = in ? t5_bucket(i - 128) : 0;
; #pragma unroll
;             for (int j = 0; j < 4; ++j) tab4[j * TC_LEN + idx] = in ? (rel_bias[(4 * kvh + j) * 32 + bk] * LOG2E + 64.0f) * KAPPA : -1.0f; }
.LBB0_1120:
	s_or_b64 exec, exec, s[8:9]
	v_add_u32_e32 v2, 0x200, v10
	v_cmp_lt_i32_e32 vcc, s31, v10
	ds_write2st64_b32 v5, v8, v9 offset0:12 offset1:18
	ds_write2st64_b32 v14, v8, v9 offset0:12 offset1:18
	v_add_u32_e32 v5, 0x800, v5
	s_or_b64 s[24:25], vcc, s[24:25]
	v_mov_b32_e32 v10, v2
	s_andn2_b64 exec, exec, s[24:25]
	s_cbranch_execz .LBB0_1131
.LBB0_1121:
	v_add_u32_e32 v14, 0x2427c, v5
	v_subrev_u32_e32 v2, 32, v10
	s_movk_i32 s8, 0x100
	v_cmp_lt_u32_e32 vcc, s8, v2
	s_movk_i32 s8, 0x101
	v_cmp_gt_u32_e64 s[8:9], s8, v2
	v_mov_b32_e32 v2, 0
	s_and_saveexec_b64 s[26:27], s[8:9]
	s_cbranch_execz .LBB0_1127
	v_add_u32_e32 v2, 0xffffff60, v10
	v_sub_u32_e32 v8, 0xa0, v10
	v_max_i32_e32 v9, v2, v8
	v_cmp_lt_u32_e64 s[8:9], s21, v10
	s_nop 1
	v_cndmask_b32_e64 v8, 0, 16, s[8:9]
	v_cmp_lt_u32_e64 s[8:9], 7, v9
	s_and_saveexec_b64 s[28:29], s[8:9]
	s_xor_b64 s[28:29], exec, s[28:29]
	s_cbranch_execz .LBB0_1124
	v_cmp_lt_u32_e64 s[8:9], 14, v9
	s_nop 1
	v_cndmask_b32_e64 v2, 8, 9, s[8:9]
	v_cmp_lt_u32_e64 s[8:9], 26, v9
	s_nop 1
	v_cndmask_b32_e64 v11, 0, 1, s[8:9]
	v_cmp_lt_u32_e64 s[8:9], 49, v9
	v_or_b32_e32 v8, v8, v11
	v_add_u32_e32 v2, v8, v2
	v_cndmask_b32_e64 v12, 0, 1, s[8:9]
	v_cmp_lt_u32_e64 s[8:9], s30, v9
	s_nop 1
	v_addc_co_u32_e64 v2, s[8:9], v2, v12, s[8:9]

; __device__ __forceinline__ void mixer_c_shared(const bf16* CQ, const bf16* CK, const bf16* CV  , bf16* O, const float* rel_bias, const float* sink, LAS unsigned char* lds, int G, int blk, int tid, int lane, int wave) {
;     ...
;         for (int idx = tid; idx < TC_LEN; idx += NWAVES * 64) { const int i = idx - TC_OFF; const bool in = (i >= 0 && i <= 256); const int bk = in ? t5_bucket(i - 128) : 0;
; #pragma unroll
;             for (int j = 0; j < 4; ++j) tab4[j * TC_LEN + idx] = in ? (rel_bias[(4 * kvh + j) * 32 + bk] * LOG2E + 64.0f) * KAPPA : -1.0f; }
.LBB0_1127:
	s_or_b64 exec, exec, s[26:27]
	s_and_saveexec_b64 s[8:9], vcc
	s_xor_b64 s[8:9], exec, s[8:9]
	ds_write2st64_b32 v5, v181, v181 offset1:6
	ds_write2st64_b32 v14, v181, v181 offset1:6
	s_or_saveexec_b64 s[8:9], s[8:9]
	v_mov_b32_e32 v8, -1.0
	v_mov_b32_e32 v9, -1.0
	s_xor_b64 exec, exec, s[8:9]
	s_cbranch_execz .LBB0_1120
	v_readlane_b32 s44, v254, 14
	v_add_u32_e32 v2, s16, v2
	v_readlane_b32 s46, v254, 16
	v_readlane_b32 s47, v254, 17
	v_readlane_b32 s45, v254, 15
	v_readlane_b32 s48, v254, 18
	v_lshl_add_u64 v[8:9], v[2:3], 2, s[46:47]
	global_load_dword v2, v[8:9], off
	global_load_dword v11, v[8:9], off offset:128
	global_load_dword v12, v[8:9], off offset:256
	global_load_dword v13, v[8:9], off offset:384
	v_readlane_b32 s49, v254, 19
	v_readlane_b32 s50, v254, 20
	v_readlane_b32 s51, v254, 21
	v_readlane_b32 s52, v254, 22
	v_readlane_b32 s53, v254, 23
	v_readlane_b32 s54, v254, 24
	v_readlane_b32 s55, v254, 25
	v_readlane_b32 s56, v254, 26
	v_readlane_b32 s57, v254, 27
	v_readlane_b32 s58, v254, 28
	v_readlane_b32 s59, v254, 29
	s_waitcnt vmcnt(3)
	v_fmamk_f32 v2, v2, 0x3fb8aa3b, v142
	s_waitcnt vmcnt(2)
	v_fmamk_f32 v11, v11, 0x3fb8aa3b, v142
	v_mul_f32_e32 v2, 0x3b000080, v2
	s_waitcnt vmcnt(0)
	v_pk_fma_f32 v[8:9], v[12:13], s[18:19], v[142:143] op_sel_hi:[1,0,0]
	v_mul_f32_e32 v11, 0x3b000080, v11
	v_pk_mul_f32 v[8:9], v[8:9], s[20:21] op_sel_hi:[1,0]
	ds_write2st64_b32 v5, v2, v11 offset1:6
	ds_write2st64_b32 v14, v2, v11 offset1:6
	s_branch .LBB0_1120

; #define BA_PACKN(p0, p1, s) do { p0.x = BA_PKN(s[0], s[1]); p0.y = BA_PKN(s[2], s[3]); p0.z = BA_PKN(s[4], s[5]); p0.w = BA_PKN(s[6], s[7]); \
;         p1.x = BA_PKN(s[8], s[9]); p1.y = BA_PKN(s[10], s[11]); p1.z = BA_PKN(s[12], s[13]); p1.w = BA_PKN(s[14], s[15]); \
;         orw |= (p0.x | p0.y | p0.z) | (p0.w | p1.x | p1.y) | (p1.z | p1.w); } while (0)
; __device__ __forceinline__ void band_branch_shared_fast(f32x16& o0, f32x16& o1, f32x4& lsum, unsigned& orw, const bf16x8 (&qf)[4],
;         const LAS unsigned char* kimg, const LAS unsigned char* vimg, int rw0, int L, int kb_first, int ntiles, const LAS float* tab, int tboff, int lane) {
;     ...
;     int kt = kt_lo;
;     for (; kt + 1 < kt_hi; kt += 2) {
;         bf16x8 kfa[4], kfb[4]; f32x16 sa, sb; s16x4 vta[8], vtb[8];
;         BA_FETCH(kfa, sa, vta, kt); BA_FETCH(kfb, sb, vtb, kt + 1);
;         __builtin_amdgcn_sched_barrier(0);
; #pragma unroll
;         for (int d0 = 0; d0 < 4; ++d0) { sa = __builtin_amdgcn_mfma_f32_32x32x16_bf16(kfa[d0], qf[d0], sa, 0, 0, 0); sb = __builtin_amdgcn_mfma_f32_32x32x16_bf16(kfb[d0], qf[d0], sb, 0, 0, 0); }
;         __builtin_amdgcn_sched_barrier(0);
;         v4u pa0, pa1, pb0, pb1; BA_PACKN(pa0, pa1, sa); BA_PACKN(pb0, pb1, sb);
;         const bf16x8 ka0 = __builtin_bit_cast(bf16x8, pa0), ka1 = __builtin_bit_cast(bf16x8, pa1), kb0 = __builtin_bit_cast(bf16x8, pb0), kb1 = __builtin_bit_cast(bf16x8, pb1);
;         BA_TILE_PV(vta, ka0, ka1); BA_TILE_PV(vtb, kb0, kb1);
;     }
.LBB0_1134:
	v_cndmask_b32_e64 v2, 0, 1, s[22:23]
	v_mov_b32_e32 v9, v148
	v_mov_b32_e32 v10, v150
	v_cmp_ne_u32_e64 s[8:9], 1, v2
	s_andn2_b64 vcc, exec, s[22:23]
	s_cbranch_vccnz .LBB0_1142
	v_mov_b32_e32 v4, 0
	v_add_u32_e32 v2, v10, v154
	v_add_u32_e32 v11, v10, v153
	v_add_u32_e32 v12, v10, v152
	v_add_u32_e32 v13, v10, v151
	v_mov_b32_e32 v8, 0
	v_mov_b32_e32 v14, v9
	v_mov_b32_e32 v15, v195
	v_and_b32_e32 v50, 4, v15
	v_mul_u32_u24_e32 v50, 0x909f, v50
	v_add_u32_e32 v15, v15, v50
	s_mov_b32 s10, s26
	v_mov_b32_e32 v5, v4
	v_mov_b32_e32 v6, v4
	v_mov_b32_e32 v7, v4
	v_mov_b32_e32 v18, v4
	v_mov_b32_e32 v19, v4
	v_mov_b32_e32 v20, v4
	v_mov_b32_e32 v21, v4
	v_mov_b32_e32 v22, v4
	v_mov_b32_e32 v23, v4
	v_mov_b32_e32 v24, v4
	v_mov_b32_e32 v25, v4
	v_mov_b32_e32 v26, v4
	v_mov_b32_e32 v27, v4
	v_mov_b32_e32 v28, v4
	v_mov_b32_e32 v29, v4
	v_mov_b32_e32 v30, v4
	v_mov_b32_e32 v31, v4
	v_mov_b32_e32 v32, v4
	v_mov_b32_e32 v33, v4
	v_mov_b32_e32 v34, v4
	v_mov_b32_e32 v35, v4
	v_mov_b32_e32 v36, v4
	v_mov_b32_e32 v37, v4
	v_mov_b32_e32 v38, v4
	v_mov_b32_e32 v39, v4
	v_mov_b32_e32 v40, v4
	v_mov_b32_e32 v41, v4
	v_mov_b32_e32 v42, v4
	v_mov_b32_e32 v43, v4
	v_mov_b32_e32 v44, v4
	v_mov_b32_e32 v45, v4
	v_mov_b32_e32 v46, v4
	v_mov_b32_e32 v47, v4
	v_mov_b32_e32 v48, v4
	v_mov_b32_e32 v49, v4
.LBB0_1136:
	v_add_u32_e32 v50, s28, v11
	v_add_u32_e32 v51, s28, v2
	v_add_u32_e32 v242, s28, v14
	v_add_u32_e32 v16, s28, v13
	v_add_u32_e32 v17, s28, v12
	ds_read_b64 v[66:67], v15
	ds_read_b64 v[68:69], v15 offset:8
	ds_read_b64 v[70:71], v15 offset:16
	ds_read_b64 v[72:73], v15 offset:24
	ds_read_b64 v[74:75], v15 offset:64
	ds_read_b64 v[76:77], v15 offset:72
	ds_read_b64 v[78:79], v15 offset:80
	ds_read_b64 v[80:81], v15 offset:88
	ds_read_b64_tr_b16 v[118:119], v242
	ds_read_b64_tr_b16 v[120:121], v242 offset:512
	ds_read_b64_tr_b16 v[124:125], v242 offset:576
	ds_read_b64_tr_b16 v[122:123], v242 offset:64
	ds_read_b64_tr_b16 v[126:127], v242 offset:2048
	ds_read_b64_tr_b16 v[128:129], v242 offset:2560
	ds_read_b64_tr_b16 v[132:133], v242 offset:2624
	ds_read_b64_tr_b16 v[130:131], v242 offset:2112
	ds_read_b128 v[134:137], v16
	ds_read_b128 v[202:205], v16 offset:4096
	ds_read_b128 v[206:209], v17
	ds_read_b128 v[210:213], v17 offset:4096
	ds_read_b128 v[214:217], v50
	ds_read_b128 v[218:221], v50 offset:4096
	ds_read_b128 v[222:225], v51
	ds_read_b128 v[226:229], v51 offset:4096
	ds_read_b64 v[50:51], v15 offset:128
	ds_read_b64 v[52:53], v15 offset:136
	ds_read_b64 v[54:55], v15 offset:144
	ds_read_b64 v[56:57], v15 offset:152
	ds_read_b64 v[58:59], v15 offset:192
	ds_read_b64 v[60:61], v15 offset:200
	ds_read_b64 v[62:63], v15 offset:208
	ds_read_b64 v[64:65], v15 offset:216
	ds_read_b64_tr_b16 v[230:231], v242 offset:4096
	ds_read_b64_tr_b16 v[232:233], v242 offset:4608
	ds_read_b64_tr_b16 v[236:237], v242 offset:4672
	ds_read_b64_tr_b16 v[234:235], v242 offset:4160
	ds_read_b64_tr_b16 v[238:239], v242 offset:6144
	ds_read_b64_tr_b16 v[240:241], v242 offset:6656
	ds_read_b64_tr_b16 v[244:245], v242 offset:6720
	ds_read_b64_tr_b16 v[242:243], v242 offset:6208
	s_mov_b32 s11, s10
	s_waitcnt lgkmcnt(14)
	v_mfma_f32_32x32x16_bf16 v[66:81], v[134:137], v[102:105], v[66:81]
	s_waitcnt lgkmcnt(8)
	v_mfma_f32_32x32x16_bf16 v[50:65], v[202:205], v[102:105], v[50:65]
	v_mfma_f32_32x32x16_bf16 v[66:81], v[206:209], v[106:109], v[66:81]
	v_mfma_f32_32x32x16_bf16 v[50:65], v[210:213], v[106:109], v[50:65]
	v_mfma_f32_32x32x16_bf16 v[66:81], v[214:217], v[110:113], v[66:81]
	v_mfma_f32_32x32x16_bf16 v[50:65], v[218:221], v[110:113], v[50:65]
	v_mfma_f32_32x32x16_bf16 v[66:81], v[222:225], v[114:117], v[66:81]
	v_mfma_f32_32x32x16_bf16 v[50:65], v[226:229], v[114:117], v[50:65]
	s_nop 10
	v_cvt_pknorm_u16_f32 v66, v66, v67
	v_cvt_pknorm_u16_f32 v67, v68, v69
	v_cvt_pknorm_u16_f32 v68, v70, v71
	v_cvt_pknorm_u16_f32 v69, v72, v73
	v_cvt_pknorm_u16_f32 v70, v74, v75
	v_cvt_pknorm_u16_f32 v71, v76, v77
	v_mfma_f32_32x32x16_bf16 v[34:49], v[118:121], v[66:69], v[34:49]
	v_cvt_pknorm_u16_f32 v72, v78, v79
	v_cvt_pknorm_u16_f32 v73, v80, v81
	v_cvt_pknorm_u16_f32 v50, v50, v51
	v_cvt_pknorm_u16_f32 v51, v52, v53
	v_cvt_pknorm_u16_f32 v52, v54, v55
	v_cvt_pknorm_u16_f32 v53, v56, v57
	v_cvt_pknorm_u16_f32 v54, v58, v59
	v_mfma_f32_32x32x16_bf16 v[18:33], v[122:125], v[66:69], v[18:33]
	v_cvt_pknorm_u16_f32 v55, v60, v61
	v_cvt_pknorm_u16_f32 v56, v62, v63
	v_cvt_pknorm_u16_f32 v57, v64, v65
	v_or3_b32 v8, v8, v73, v72
	v_or3_b32 v8, v8, v70, v69
	v_or3_b32 v8, v8, v71, v67
	v_or3_b32 v8, v8, v66, v68
	v_mfma_f32_32x32x16_bf16 v[34:49], v[126:129], v[70:73], v[34:49]
	v_or3_b32 v8, v8, v57, v56
	v_or3_b32 v8, v8, v54, v53
	s_add_i32 s10, s10, 2
	s_add_i32 s11, s11, 3
	v_or3_b32 v8, v8, v55, v51
	v_add_u32_e32 v15, 0x100, v15
	v_add_u32_e32 v14, 0x2000, v14
	v_mfma_f32_32x32x16_bf16 v[18:33], v[130:133], v[70:73], v[18:33]
	v_add_u32_e32 v2, 0x2000, v2
	v_add_u32_e32 v11, 0x2000, v11
	v_add_u32_e32 v12, 0x2000, v12
	v_add_u32_e32 v13, 0x2000, v13
	s_cmp_lt_i32 s11, s27
	v_or3_b32 v8, v8, v50, v52
	s_waitcnt lgkmcnt(6)
	v_mfma_f32_32x32x16_bf16 v[34:49], v[230:233], v[50:53], v[34:49]
	s_waitcnt lgkmcnt(4)
	v_mfma_f32_32x32x16_bf16 v[18:33], v[234:237], v[50:53], v[18:33]
	v_mfma_f32_16x16x32_bf16 v[4:7], v[82:85], v[66:69], v[4:7]
	v_mfma_f32_16x16x32_bf16 v[4:7], v[82:85], v[70:73], v[4:7]
	s_waitcnt lgkmcnt(2)
	v_mfma_f32_32x32x16_bf16 v[34:49], v[238:241], v[54:57], v[34:49]
	s_waitcnt lgkmcnt(0)
	v_mfma_f32_32x32x16_bf16 v[18:33], v[242:245], v[54:57], v[18:33]
	v_mfma_f32_16x16x32_bf16 v[4:7], v[82:85], v[50:53], v[4:7]
	v_mfma_f32_16x16x32_bf16 v[4:7], v[82:85], v[54:57], v[4:7]
	s_cbranch_scc1 .LBB0_1136
	s_mul_i32 s11, s25, 0x600
	s_add_i32 s33, s11, 0
	s_cmp_ge_i32 s10, s27
	s_cbranch_scc1 .LBB0_1139
; #define BA_PACKN(p0, p1, s) do { p0.x = BA_PKN(s[0], s[1]); p0.y = BA_PKN(s[2], s[3]); p0.z = BA_PKN(s[4], s[5]); p0.w = BA_PKN(s[6], s[7]); \
;         p1.x = BA_PKN(s[8], s[9]); p1.y = BA_PKN(s[10], s[11]); p1.z = BA_PKN(s[12], s[13]); p1.w = BA_PKN(s[14], s[15]); \
;         orw |= (p0.x | p0.y | p0.z) | (p0.w | p1.x | p1.y) | (p1.z | p1.w); } while (0)
; __device__ __forceinline__ void band_branch_shared_fast(f32x16& o0, f32x16& o1, f32x4& lsum, unsigned& orw, const bf16x8 (&qf)[4],
;         const LAS unsigned char* kimg, const LAS unsigned char* vimg, int rw0, int L, int kb_first, int ntiles, const LAS float* tab, int tboff, int lane) {
;     ...
;     if (kt < kt_hi) {
;         bf16x8 kfa[4]; f32x16 sa; s16x4 vta[8];
;         BA_FETCH(kfa, sa, vta, kt);
;         __builtin_amdgcn_sched_barrier(0);
; #pragma unroll
;         for (int d0 = 0; d0 < 4; ++d0) sa = __builtin_amdgcn_mfma_f32_32x32x16_bf16(kfa[d0], qf[d0], sa, 0, 0, 0);
;         __builtin_amdgcn_sched_barrier(0);
;         v4u pa0, pa1; BA_PACKN(pa0, pa1, sa);
;         const bf16x8 ka0 = __builtin_bit_cast(bf16x8, pa0), ka1 = __builtin_bit_cast(bf16x8, pa1);
;         BA_TILE_PV(vta, ka0, ka1);
;     }
.LBB0_1138:
	s_lshl_b32 s11, s10, 12
	v_add_u32_e32 v2, s11, v10
	s_add_i32 s16, s33, s29
	s_lshl_b32 s10, s10, 7
	v_add_u32_e32 v10, v2, v151
	v_add_u32_e32 v14, v2, v152
	v_add_u32_e32 v50, v2, v153
	v_add_u32_e32 v2, v2, v154
	s_add_i32 s16, s16, s10
	ds_read_b128 v[10:13], v10
	ds_read_b128 v[14:17], v14
	ds_read_b128 v[66:69], v50
	ds_read_b128 v[70:73], v2
	v_lshl_add_u32 v2, v194, 2, s16
	v_and_b32_e32 v64, 4, v2
	v_mul_u32_u24_e32 v64, 0x909f, v64
	v_add_u32_e32 v2, v2, v64
	ds_read_b64 v[50:51], v2 offset:640
	ds_read_b64 v[52:53], v2 offset:648
	ds_read_b64 v[54:55], v2 offset:656
	ds_read_b64 v[56:57], v2 offset:664
	ds_read_b64 v[58:59], v2 offset:704
	ds_read_b64 v[60:61], v2 offset:712
	ds_read_b64 v[62:63], v2 offset:720
	ds_read_b64 v[64:65], v2 offset:728
	v_add_u32_e32 v2, s11, v9
	ds_read_b64_tr_b16 v[74:75], v2
	ds_read_b64_tr_b16 v[76:77], v2 offset:512
	ds_read_b64_tr_b16 v[80:81], v2 offset:576
	ds_read_b64_tr_b16 v[78:79], v2 offset:64
	ds_read_b64_tr_b16 v[118:119], v2 offset:2048
	ds_read_b64_tr_b16 v[120:121], v2 offset:2560
	ds_read_b64_tr_b16 v[124:125], v2 offset:2624
	ds_read_b64_tr_b16 v[122:123], v2 offset:2112
	s_waitcnt lgkmcnt(8)
	v_mfma_f32_32x32x16_bf16 v[50:65], v[10:13], v[102:105], v[50:65]
	v_mfma_f32_32x32x16_bf16 v[50:65], v[14:17], v[106:109], v[50:65]
	v_mfma_f32_32x32x16_bf16 v[50:65], v[66:69], v[110:113], v[50:65]
	v_mfma_f32_32x32x16_bf16 v[50:65], v[70:73], v[114:117], v[50:65]
	s_nop 11
	v_cvt_pknorm_u16_f32 v10, v50, v51
	v_cvt_pknorm_u16_f32 v11, v52, v53
	v_cvt_pknorm_u16_f32 v12, v54, v55
	v_cvt_pknorm_u16_f32 v13, v56, v57
	v_cvt_pknorm_u16_f32 v14, v58, v59
	v_cvt_pknorm_u16_f32 v15, v60, v61
	s_waitcnt lgkmcnt(6)
	v_mfma_f32_32x32x16_bf16 v[34:49], v[74:77], v[10:13], v[34:49]
	v_cvt_pknorm_u16_f32 v16, v62, v63
	v_cvt_pknorm_u16_f32 v17, v64, v65
	v_or3_b32 v2, v8, v17, v16
	v_or3_b32 v2, v2, v14, v13
	v_or3_b32 v2, v2, v15, v11
	v_or3_b32 v8, v2, v10, v12
	s_waitcnt lgkmcnt(4)
	v_mfma_f32_32x32x16_bf16 v[18:33], v[78:81], v[10:13], v[18:33]
	s_waitcnt lgkmcnt(2)
	v_mfma_f32_32x32x16_bf16 v[34:49], v[118:121], v[14:17], v[34:49]
	v_mfma_f32_16x16x32_bf16 v[4:7], v[82:85], v[10:13], v[4:7]
	s_waitcnt lgkmcnt(0)
	v_mfma_f32_32x32x16_bf16 v[18:33], v[122:125], v[14:17], v[18:33]
	v_mfma_f32_16x16x32_bf16 v[4:7], v[82:85], v[14:17], v[4:7]
